# mixer phase: retention workgroups (done ~25 us before the HGRN2 ones) use the pipelined converter in their tail; HGRN2 units signal 4 chunks before their end
# baseline (speedup 1.0000x reference)
.LBB0_465:
	s_waitcnt lgkmcnt(0)
	s_barrier
	ds_read_b128 v[10:13], v127
	ds_read_b128 v[14:17], v127 offset:64
	ds_read_b128 v[56:59], v127 offset:128
	ds_read_b128 v[60:63], v127 offset:192
	ds_read_b128 v[64:67], v128 offset:17408
	ds_read_b128 v[68:71], v128 offset:17472
	ds_read_b128 v[72:75], v128 offset:17536
	ds_read_b128 v[76:79], v128 offset:17600
	ds_read_b128 v[176:179], v128 offset:21760
	ds_read_b128 v[180:183], v128 offset:21824
	ds_read_b128 v[184:187], v128 offset:21888
	ds_read_b128 v[188:191], v128 offset:21952
	s_waitcnt lgkmcnt(7)
	v_mfma_f32_16x16x32_bf16 v[2:5], v[64:67], v[10:13], 0
	s_waitcnt lgkmcnt(6)
	v_mfma_f32_16x16x32_bf16 v[2:5], v[68:71], v[14:17], v[2:5]
	s_waitcnt lgkmcnt(3)
	v_mfma_f32_16x16x32_bf16 v[6:9], v[176:179], v[10:13], 0
	v_mfma_f32_16x16x32_bf16 v[2:5], v[72:75], v[56:59], v[2:5]
	s_waitcnt lgkmcnt(2)
	v_mfma_f32_16x16x32_bf16 v[6:9], v[180:183], v[14:17], v[6:9]
	v_mfma_f32_16x16x32_bf16 v[2:5], v[76:79], v[60:63], v[2:5]
	s_waitcnt lgkmcnt(1)
	v_mfma_f32_16x16x32_bf16 v[6:9], v[184:187], v[56:59], v[6:9]
	s_waitcnt lgkmcnt(0)
	v_mfma_f32_16x16x32_bf16 v[6:9], v[188:191], v[60:63], v[6:9]
	s_nop 6
	v_cndmask_b32_e64 v56, v2, 0, s[44:45]
	v_cndmask_b32_e64 v57, 0, v3, s[46:47]
	v_cndmask_b32_e64 v58, v4, 0, s[48:49]
	v_cndmask_b32_e64 v59, v5, 0, s[50:51]
	v_cvt_pk_bf16_f32 v56, v56, v57
	v_cvt_pk_bf16_f32 v57, v58, v59
	ds_write_b64 v129, v[56:57]
	v_cndmask_b32_e64 v6, v6, 0, s[52:53]
	v_cndmask_b32_e64 v7, 0, v7, s[54:55]
	v_cndmask_b32_e64 v8, v8, 0, s[56:57]
	v_cndmask_b32_e64 v9, v9, 0, s[58:59]
	v_cvt_pk_bf16_f32 v6, v6, v7
	v_cvt_pk_bf16_f32 v7, v8, v9
	ds_write_b64 v130, v[6:7]
	s_waitcnt lgkmcnt(0)
	s_barrier
	ds_read_b128 v[10:13], v131
	ds_read_b128 v[14:17], v132
	ds_read_b128 v[56:59], v133
	ds_read_b128 v[60:63], v131 offset:64
	ds_read_b128 v[64:67], v132 offset:64
	ds_read_b128 v[68:71], v133 offset:64
	ds_read_b128 v[72:75], v138
	ds_read_b128 v[76:79], v134 offset:52224
	ds_read_b128 v[176:179], v137
	ds_read_b128 v[180:183], v137 offset:2304
	ds_read_b128 v[184:187], v137 offset:4608
	ds_read_b128 v[188:191], v137 offset:6912
	ds_read_b128 v[200:203], v134 offset:52288
	ds_read_b128 v[204:207], v137 offset:64
	ds_read_b128 v[208:211], v137 offset:2368
	s_waitcnt lgkmcnt(13)
	v_mfma_f32_16x16x32_bf16 v[6:9], v[10:13], v[14:17], 0
	s_waitcnt lgkmcnt(12)
	v_mfma_f32_16x16x32_bf16 v[2:5], v[10:13], v[56:59], 0
	ds_read_b128 v[212:215], v137 offset:4672
	ds_read_b128 v[220:223], v137 offset:6976
	ds_read_b128 v[224:227], v135
	s_waitcnt lgkmcnt(13)
	v_mfma_f32_16x16x32_bf16 v[6:9], v[60:63], v[64:67], v[6:9]
	s_waitcnt lgkmcnt(12)
	v_mfma_f32_16x16x32_bf16 v[2:5], v[60:63], v[68:71], v[2:5]
	ds_read_b128 v[232:235], v128
	ds_read_b128 v[236:239], v136
	ds_read_b128 v[14:17], v135 offset:64
	s_waitcnt lgkmcnt(14)
	v_pk_mul_f32 v[22:23], v[22:23], v[72:73]
	v_pk_mul_f32 v[24:25], v[24:25], v[74:75]
	v_pk_mul_f32 v[26:27], v[26:27], v[72:73]
	v_pk_mul_f32 v[28:29], v[28:29], v[74:75]
	v_pk_mul_f32 v[30:31], v[30:31], v[72:73]
	v_pk_mul_f32 v[32:33], v[32:33], v[74:75]
	v_pk_mul_f32 v[34:35], v[34:35], v[72:73]
	v_pk_mul_f32 v[36:37], v[36:37], v[74:75]
	s_waitcnt lgkmcnt(12)
	v_mfma_f32_16x16x32_bf16 v[22:25], v[76:79], v[176:179], v[22:25]
	s_waitcnt lgkmcnt(11)
	v_mfma_f32_16x16x32_bf16 v[26:29], v[76:79], v[180:183], v[26:29]
	s_waitcnt lgkmcnt(10)
	v_mfma_f32_16x16x32_bf16 v[30:33], v[76:79], v[184:187], v[30:33]
	s_waitcnt lgkmcnt(9)
	v_mfma_f32_16x16x32_bf16 v[34:37], v[76:79], v[188:191], v[34:37]
	ds_read_b128 v[10:13], v128 offset:64
	ds_read_b128 v[56:59], v136 offset:64
	ds_read_b128 v[64:67], v135 offset:128
	ds_read_b128 v[60:63], v128 offset:128
	s_waitcnt lgkmcnt(11)
	v_mfma_f32_16x16x32_bf16 v[22:25], v[200:203], v[204:207], v[22:25]
	s_waitcnt lgkmcnt(10)
	v_mfma_f32_16x16x32_bf16 v[26:29], v[200:203], v[208:211], v[26:29]
	ds_read_b128 v[68:71], v136 offset:128
	ds_read_b128 v[72:75], v135 offset:192
	s_waitcnt lgkmcnt(11)
	v_mfma_f32_16x16x32_bf16 v[30:33], v[200:203], v[212:215], v[30:33]
	s_waitcnt lgkmcnt(10)
	v_mfma_f32_16x16x32_bf16 v[34:37], v[200:203], v[220:223], v[34:37]
	ds_read_b128 v[176:179], v128 offset:192
	ds_read_b128 v[180:183], v136 offset:192
	s_waitcnt lgkmcnt(10)
	v_mfma_f32_16x16x32_bf16 v[6:9], v[224:227], v[232:235], v[6:9]
	s_waitcnt lgkmcnt(9)
	v_mfma_f32_16x16x32_bf16 v[2:5], v[224:227], v[236:239], v[2:5]
	s_waitcnt lgkmcnt(7)
	v_mfma_f32_16x16x32_bf16 v[6:9], v[14:17], v[10:13], v[6:9]
	s_waitcnt lgkmcnt(6)
	v_mfma_f32_16x16x32_bf16 v[2:5], v[14:17], v[56:59], v[2:5]
	s_waitcnt lgkmcnt(4)
	v_mfma_f32_16x16x32_bf16 v[6:9], v[64:67], v[60:63], v[6:9]
	s_waitcnt lgkmcnt(3)
	v_mfma_f32_16x16x32_bf16 v[2:5], v[64:67], v[68:71], v[2:5]
	s_waitcnt lgkmcnt(1)
	v_mfma_f32_16x16x32_bf16 v[6:9], v[72:75], v[176:179], v[6:9]
	s_waitcnt lgkmcnt(0)
	v_mfma_f32_16x16x32_bf16 v[2:5], v[72:75], v[180:183], v[2:5]
	v_add_u32_e32 v57, s24, v118
	v_add_u32_e32 v56, s4, v109
	v_add_u32_e32 v58, 0x7ff, v57
	s_cmpk_eq_i32 s4, 0x6c0
	s_cselect_b32 s98, 1, 0
	s_add_i32 s4, s4, 64
	s_sub_i32 s24, s24, 64
	v_cndmask_b32_e64 v58, v58, v56, s[76:77]
	s_cmpk_eq_i32 s4, 0x800
	s_waitcnt vmcnt(1)
	s_cselect_b32 s99, 1, 0
	s_cmp_eq_u32 s98, 0
	s_cbranch_scc1 .Les_p3_rest
	v_writelane_b32 v255, 1, 63
	v_readfirstlane_b32 s98, v0
	s_cmp_lg_u32 s98, 0
	s_cbranch_scc1 .Les_p3_rest
	v_readlane_b32 s40, v255, 18
	s_lshl_b32 s40, s40, 10
	s_add_u32 s40, s40, 0x5200
	v_readlane_b32 s41, v255, 5
	s_add_u32 s40, s40, s41
	v_readlane_b32 s41, v255, 6
	s_addc_u32 s41, s41, 0
	s_mov_b64 exec, 1
	global_atomic_add v195, v197, s[40:41]
	s_mov_b64 exec, -1
.Les_p3_rest:
	s_cmp_lg_u32 s99, 0
	s_nop 0
	v_cvt_pk_bf16_f32 v6, v6, v7
	v_cvt_pk_bf16_f32 v7, v8, v9
	v_or_b32_e32 v8, s84, v58
	v_ashrrev_i32_e32 v9, 31, v8
	v_lshl_add_u64 v[8:9], v[8:9], 0, s[2:3]
	v_mad_u64_u32 v[14:15], s[8:9], v8, s11, v[54:55]
	v_mad_i32_i24 v15, v9, s11, v15
	global_store_dwordx2 v[14:15], v[6:7], off
	v_add_u32_e32 v6, 16, v56
	v_add_u32_e32 v7, 0x7ef, v57
	v_cndmask_b32_e64 v6, v7, v6, s[76:77]
	v_cvt_pk_bf16_f32 v2, v2, v3
	v_cvt_pk_bf16_f32 v3, v4, v5
	v_or_b32_e32 v4, s84, v6
	v_ashrrev_i32_e32 v5, 31, v4
	v_lshl_add_u64 v[4:5], v[4:5], 0, s[2:3]
	v_mad_u64_u32 v[6:7], s[8:9], v4, s11, v[54:55]
	v_mad_i32_i24 v7, v5, s11, v7
	global_store_dwordx2 v[6:7], v[2:3], off
	s_cbranch_scc1 .LBB0_448

.LBB0_483:
	v_readlane_b32 s100, v255, 63
	v_writelane_b32 v255, 0, 63
	v_readlane_b32 s0, v255, 18
	v_readlane_b32 s1, v255, 19
	s_lshl_b32 s0, s0, 8
	s_ashr_i32 s1, s0, 31
	s_add_u32 s6, s22, 0x5000
	s_addc_u32 s7, s23, 0
	s_lshl_b64 s[0:1], s[0:1], 2
	s_add_u32 s26, s6, s0
	s_addc_u32 s27, s7, s1
	s_waitcnt vmcnt(0) lgkmcnt(0)
	s_barrier
	s_mov_b64 s[8:9], exec
	v_readlane_b32 s0, v253, 4
	v_readlane_b32 s1, v253, 5
	s_and_b64 s[0:1], s[8:9], s[0:1]
	s_mov_b64 exec, s[0:1]
	s_cbranch_execz .LBB0_486
	s_cmp_lg_u32 s100, 0
	s_cbranch_scc1 .LBB0_486
	s_mov_b64 s[28:29], exec
	v_mbcnt_lo_u32_b32 v1, s28, 0
	v_mbcnt_hi_u32_b32 v1, s29, v1
	v_cmp_eq_u32_e32 vcc, 0, v1
	s_and_b64 s[0:1], exec, vcc
	s_mov_b64 exec, s[0:1]
	s_cbranch_execz .LBB0_486
	s_bcnt1_i32_b64 s0, s[28:29]
	v_mov_b32_e32 v1, s0
	global_atomic_add v195, v1, s[26:27] offset:512
.LBB0_486:
	s_or_b64 exec, exec, s[8:9]
	v_readlane_b32 s33, v255, 12
	s_cmpk_ge_u32 s33, 192
	s_cbranch_scc1 .Lfc_p3_go
	s_bitcmp1_b32 s33, 2
	s_cbranch_scc1 .Lfc_p3_skip
.Lfc_p3_go:
	v_lshrrev_b32_e32 v1, 4, v0
	v_lshlrev_b32_e32 v1, 1, v1
	v_and_b32_e32 v2, 15, v0
	v_lshlrev_b32_e32 v2, 4, v2
	v_mov_b32_e32 v3, 0
	v_and_b32_e32 v4, 7, v0
	v_lshlrev_b32_e32 v4, 3, v4
	v_mov_b32_e32 v5, 0
	v_lshrrev_b32_e32 v6, 3, v0
	v_mov_b32_e32 v7, 2
	v_mov_b32_e32 v8, 0x42800000
	v_mov_b32_e32 v9, 0x42800000
	v_and_b32_e32 v16, 15, v0
	v_mul_u32_u24_e32 v16, 0x110, v16
	v_add_u32_e32 v16, v16, v1
	v_mul_u32_u24_e32 v17, 0x44, v6
	v_add_u32_e32 v17, v17, v4
	v_mov_b32_e32 v13, 0x25a00
	v_readlane_b32 s56, v255, 5
	v_readlane_b32 s57, v255, 6
	v_readlane_b32 s13, v255, 7
	v_readlane_b32 s8, v255, 14
	v_readlane_b32 s9, v255, 15
	v_readlane_b32 s33, v255, 18
	s_load_dwordx2 s[36:37], s[8:9], 0x30
	s_load_dwordx2 s[38:39], s[8:9], 0x48
	s_load_dwordx4 s[40:43], s[8:9], 0x78
	s_load_dwordx2 s[44:45], s[8:9], 0x88
	s_add_u32 s58, s56, 0x5000
	s_addc_u32 s59, s57, 0
	s_lshl_b32 s33, s33, 10
	s_add_i32 s33, s33, 512
	s_add_u32 s60, s58, s33
	s_addc_u32 s61, s59, 0
	s_waitcnt lgkmcnt(0)
	v_cmp_eq_u32_e32 vcc, 0, v0
	s_and_saveexec_b64 s[16:17], vcc
	s_cbranch_execz .Lfc_p3_init_done
	global_load_dword v11, v195, s[60:61] sc1
	s_mov_b32 s14, -1
	s_mov_b32 s25, -1
	s_waitcnt vmcnt(0)
	v_readfirstlane_b32 s33, v11
	s_cmp_ge_u32 s33, s13
	s_cbranch_scc1 .Lfc_p3_init_w
	v_mov_b32_e32 v12, 4
	global_atomic_add v10, v195, v12, s[58:59] sc0
	s_waitcnt vmcnt(0)
	v_readfirstlane_b32 s33, v10
	s_cmpk_lt_u32 s33, 0x4c40
	s_cselect_b32 s14, s33, -1
	s_add_i32 s33, s33, 2
	s_cmpk_lt_u32 s33, 0x4c40
	s_cselect_b32 s25, s33, -1
